# epilogue de-serialisation: the per-row-panel rs cache fill of the gate/up and in-proj epilogues issues its 16 partial-sum loads together and runs one reduction pipeline (8 load round trips and 16 LDS
# speedup vs baseline: 1.0012x; 1.0012x over previous
; __device__ __forceinline__ float row_rs(const float* ssq, int row, int fq) {
;     const float* pp = ssq + (size_t)row * 32 + 8 * fq; const f32x4 p0 = *(const f32x4*)pp, p1 = *(const f32x4*)(pp + 4);
;     float s = ((p0[0] + p0[1]) + (p0[2] + p0[3])) + ((p1[0] + p1[1]) + (p1[2] + p1[3]));
;     s += __shfl_xor(s, 16); s += __shfl_xor(s, 32);
;     return __builtin_amdgcn_rsqf(s * (1.0f / 2048.0f) + 1e-6f);
; }
;     __device__ __forceinline__ void operator()(const f32x4 (&acc)[2][2][4][2], const Unit& u, int wr, int wc, int fr, int fq) const {
;     ...
;         if (u.pm != cpm) { cpm = u.pm;
; #pragma unroll
;             for (int ai = 0; ai < 2; ++ai)
; #pragma unroll
;                 for (int m = 0; m < 4; ++m) { const float r = row_rs(ssq, row0 + ai * HALF + m * 16, fq); if (fq == 0) my[(ai * 4 + m) * 16] = r; } }
.LBB0_133:
	v_lshl_add_u32 v144, s43, 8, v3
	s_mov_b64 s[4:5], -1
	s_cmp_lg_u32 s43, s3
	v_ashrrev_i32_e32 v145, 31, v144
	s_cbranch_scc0 .LBB0_151
	v_and_b32_e32 v155, 64, v210
	v_xor_b32_e32 v154, 16, v210
	v_add_u32_e32 v155, 64, v155
	v_cmp_lt_i32_e32 vcc, v154, v155
	v_cndmask_b32_e32 v154, v210, v154, vcc
	v_lshlrev_b32_e32 v142, 2, v154
	v_xor_b32_e32 v154, 32, v210
	v_cmp_lt_i32_e32 vcc, v154, v155
	v_cndmask_b32_e32 v154, v210, v154, vcc
	v_lshlrev_b32_e32 v143, 2, v154
	v_lshlrev_b64 v[140:141], 7, v[144:145]
	v_lshl_add_u64 v[140:141], v[136:137], 0, v[140:141]
	global_load_dwordx4 v[164:167], v[140:141], off
	global_load_dwordx4 v[168:171], v[140:141], off offset:16
	v_add_u32_e32 v140, 0x10, v144
	v_ashrrev_i32_e32 v141, 31, v140
	v_lshlrev_b64 v[140:141], 7, v[140:141]
	v_lshl_add_u64 v[140:141], v[136:137], 0, v[140:141]
	global_load_dwordx4 v[172:175], v[140:141], off
	global_load_dwordx4 v[176:179], v[140:141], off offset:16
	v_add_u32_e32 v140, 0x20, v144
	v_ashrrev_i32_e32 v141, 31, v140
	v_lshlrev_b64 v[140:141], 7, v[140:141]
	v_lshl_add_u64 v[140:141], v[136:137], 0, v[140:141]
	global_load_dwordx4 v[180:183], v[140:141], off
	global_load_dwordx4 v[190:193], v[140:141], off offset:16
	v_add_u32_e32 v140, 0x30, v144
	v_ashrrev_i32_e32 v141, 31, v140
	v_lshlrev_b64 v[140:141], 7, v[140:141]
	v_lshl_add_u64 v[140:141], v[136:137], 0, v[140:141]
	global_load_dwordx4 v[194:197], v[140:141], off
	global_load_dwordx4 v[198:201], v[140:141], off offset:16
	v_add_u32_e32 v140, 0x80, v144
	v_ashrrev_i32_e32 v141, 31, v140
	v_lshlrev_b64 v[140:141], 7, v[140:141]
	v_lshl_add_u64 v[140:141], v[136:137], 0, v[140:141]
	global_load_dwordx4 v[202:205], v[140:141], off
	global_load_dwordx4 v[206:209], v[140:141], off offset:16
	v_add_u32_e32 v140, 0x90, v144
	v_ashrrev_i32_e32 v141, 31, v140
	v_lshlrev_b64 v[140:141], 7, v[140:141]
	v_lshl_add_u64 v[140:141], v[136:137], 0, v[140:141]
	global_load_dwordx4 v[216:219], v[140:141], off
	global_load_dwordx4 v[220:223], v[140:141], off offset:16
	v_add_u32_e32 v140, 0xa0, v144
	v_ashrrev_i32_e32 v141, 31, v140
	v_lshlrev_b64 v[140:141], 7, v[140:141]
	v_lshl_add_u64 v[140:141], v[136:137], 0, v[140:141]
	global_load_dwordx4 v[224:227], v[140:141], off
	global_load_dwordx4 v[228:231], v[140:141], off offset:16
	v_add_u32_e32 v140, 0xb0, v144
	v_ashrrev_i32_e32 v141, 31, v140
	v_lshlrev_b64 v[140:141], 7, v[140:141]
	v_lshl_add_u64 v[140:141], v[136:137], 0, v[140:141]
	global_load_dwordx4 v[232:235], v[140:141], off
	global_load_dwordx4 v[236:239], v[140:141], off offset:16
	s_waitcnt vmcnt(14)
	v_add_f32_e32 v146, v164, v165
	v_add_f32_e32 v154, v166, v167
	v_add_f32_e32 v155, v168, v169
	v_add_f32_e32 v156, v170, v171
	v_add_f32_e32 v146, v146, v154
	v_add_f32_e32 v154, v155, v156
	v_add_f32_e32 v146, v146, v154
	ds_bpermute_b32 v240, v142, v146
	s_waitcnt vmcnt(12)
	v_add_f32_e32 v147, v172, v173
	v_add_f32_e32 v154, v174, v175
	v_add_f32_e32 v155, v176, v177
	v_add_f32_e32 v156, v178, v179
	v_add_f32_e32 v147, v147, v154
	v_add_f32_e32 v154, v155, v156
	v_add_f32_e32 v147, v147, v154
	ds_bpermute_b32 v241, v142, v147
	s_waitcnt vmcnt(10)
	v_add_f32_e32 v148, v180, v181
	v_add_f32_e32 v154, v182, v183
	v_add_f32_e32 v155, v190, v191
	v_add_f32_e32 v156, v192, v193
	v_add_f32_e32 v148, v148, v154
	v_add_f32_e32 v154, v155, v156
	v_add_f32_e32 v148, v148, v154
	ds_bpermute_b32 v242, v142, v148
	s_waitcnt vmcnt(8)
	v_add_f32_e32 v149, v194, v195
	v_add_f32_e32 v154, v196, v197
	v_add_f32_e32 v155, v198, v199
	v_add_f32_e32 v156, v200, v201
	v_add_f32_e32 v149, v149, v154
	v_add_f32_e32 v154, v155, v156
	v_add_f32_e32 v149, v149, v154
	ds_bpermute_b32 v243, v142, v149
	s_waitcnt vmcnt(6)
	v_add_f32_e32 v150, v202, v203
	v_add_f32_e32 v154, v204, v205
	v_add_f32_e32 v155, v206, v207
	v_add_f32_e32 v156, v208, v209
	v_add_f32_e32 v150, v150, v154
	v_add_f32_e32 v154, v155, v156
	v_add_f32_e32 v150, v150, v154
	ds_bpermute_b32 v244, v142, v150
	s_waitcnt vmcnt(4)
	v_add_f32_e32 v151, v216, v217
	v_add_f32_e32 v154, v218, v219
	v_add_f32_e32 v155, v220, v221
	v_add_f32_e32 v156, v222, v223
	v_add_f32_e32 v151, v151, v154
	v_add_f32_e32 v154, v155, v156
	v_add_f32_e32 v151, v151, v154
	ds_bpermute_b32 v245, v142, v151
	s_waitcnt vmcnt(2)
	v_add_f32_e32 v152, v224, v225
	v_add_f32_e32 v154, v226, v227
	v_add_f32_e32 v155, v228, v229
	v_add_f32_e32 v156, v230, v231
	v_add_f32_e32 v152, v152, v154
	v_add_f32_e32 v154, v155, v156
	v_add_f32_e32 v152, v152, v154
	ds_bpermute_b32 v246, v142, v152
	s_waitcnt vmcnt(0)
	v_add_f32_e32 v153, v232, v233
	v_add_f32_e32 v154, v234, v235
	v_add_f32_e32 v155, v236, v237
	v_add_f32_e32 v156, v238, v239
	v_add_f32_e32 v153, v153, v154
	v_add_f32_e32 v154, v155, v156
	v_add_f32_e32 v153, v153, v154
	ds_bpermute_b32 v247, v142, v153
	s_waitcnt lgkmcnt(0)
	v_add_f32_e32 v146, v146, v240
	ds_bpermute_b32 v240, v143, v146
	v_add_f32_e32 v147, v147, v241
	ds_bpermute_b32 v241, v143, v147
	v_add_f32_e32 v148, v148, v242
	ds_bpermute_b32 v242, v143, v148
	v_add_f32_e32 v149, v149, v243
	ds_bpermute_b32 v243, v143, v149
	v_add_f32_e32 v150, v150, v244
	ds_bpermute_b32 v244, v143, v150
	v_add_f32_e32 v151, v151, v245
	ds_bpermute_b32 v245, v143, v151
	v_add_f32_e32 v152, v152, v246
	ds_bpermute_b32 v246, v143, v152
	v_add_f32_e32 v153, v153, v247
	ds_bpermute_b32 v247, v143, v153
	s_and_saveexec_b64 s[4:5], s[6:7]
	s_cbranch_execz .Lrsfill_gu_skip
	s_waitcnt lgkmcnt(0)
	v_add_f32_e32 v146, v146, v240
	v_fmamk_f32 v146, v146, 0x3a000000, v213
	v_rsq_f32_e32 v146, v146
	ds_write_b32 v161, v146
	v_add_f32_e32 v147, v147, v241
	v_fmamk_f32 v147, v147, 0x3a000000, v213
	v_rsq_f32_e32 v147, v147
	ds_write_b32 v161, v147 offset:64
	v_add_f32_e32 v148, v148, v242
	v_fmamk_f32 v148, v148, 0x3a000000, v213
	v_rsq_f32_e32 v148, v148
	ds_write_b32 v161, v148 offset:128
	v_add_f32_e32 v149, v149, v243
	v_fmamk_f32 v149, v149, 0x3a000000, v213
	v_rsq_f32_e32 v149, v149
	ds_write_b32 v161, v149 offset:192
	v_add_f32_e32 v150, v150, v244
	v_fmamk_f32 v150, v150, 0x3a000000, v213
	v_rsq_f32_e32 v150, v150
	ds_write_b32 v161, v150 offset:256
	v_add_f32_e32 v151, v151, v245
	v_fmamk_f32 v151, v151, 0x3a000000, v213
	v_rsq_f32_e32 v151, v151
	ds_write_b32 v161, v151 offset:320
	v_add_f32_e32 v152, v152, v246
	v_fmamk_f32 v152, v152, 0x3a000000, v213
	v_rsq_f32_e32 v152, v152
	ds_write_b32 v161, v152 offset:384
	v_add_f32_e32 v153, v153, v247
	v_fmamk_f32 v153, v153, 0x3a000000, v213
	v_rsq_f32_e32 v153, v153
	ds_write_b32 v161, v153 offset:448
;     __device__ __forceinline__ void operator()(const f32x4 (&acc)[2][2][4][2], const Unit& u, int wr, int wc, int fr, int fq) const {
;     ...
;         if (u.pm != cpm) { cpm = u.pm;
; #pragma unroll
;             for (int ai = 0; ai < 2; ++ai)
; #pragma unroll
;                 for (int m = 0; m < 4; ++m) { const float r = row_rs(ssq, row0 + ai * HALF + m * 16, fq); if (fq == 0) my[(ai * 4 + m) * 16] = r; } }
.Lrsfill_gu_skip:
	s_or_b64 exec, exec, s[4:5]
	s_waitcnt lgkmcnt(0)
	v_or_b32_e32 v156, 16, v144
	v_or_b32_e32 v154, 32, v144
	v_or_b32_e32 v152, 48, v144
	v_add_u32_e32 v150, 0x80, v144
	v_add_u32_e32 v148, 0x90, v144
	v_add_u32_e32 v146, 0xa0, v144
	v_add_u32_e32 v140, 0xb0, v144
	v_ashrrev_i32_e32 v157, 31, v156
	v_ashrrev_i32_e32 v155, 31, v154
	v_ashrrev_i32_e32 v153, 31, v152
	v_ashrrev_i32_e32 v151, 31, v150
	v_ashrrev_i32_e32 v149, 31, v148
	v_ashrrev_i32_e32 v147, 31, v146
	v_ashrrev_i32_e32 v141, 31, v140
	s_mov_b64 s[4:5], 0

; __device__ __forceinline__ float row_rs(const float* ssq, int row, int fq) {
;     const float* pp = ssq + (size_t)row * 32 + 8 * fq; const f32x4 p0 = *(const f32x4*)pp, p1 = *(const f32x4*)(pp + 4);
;     float s = ((p0[0] + p0[1]) + (p0[2] + p0[3])) + ((p1[0] + p1[1]) + (p1[2] + p1[3]));
;     s += __shfl_xor(s, 16); s += __shfl_xor(s, 32);
;     return __builtin_amdgcn_rsqf(s * (1.0f / 2048.0f) + 1e-6f);
; }
;     __device__ __forceinline__ void operator()(const f32x4 (&acc)[2][2][4][2], const Unit& u, int wr, int wc, int fr, int fq) const {
;     ...
;         if (u.pm != cpm) { cpm = u.pm;
; #pragma unroll
;             for (int ai = 0; ai < 2; ++ai)
; #pragma unroll
;                 for (int m = 0; m < 4; ++m) { const float r = row_rs(ssq, row0 + ai * HALF + m * 16, fq); if (fq == 0) my[(ai * 4 + m) * 16] = r; } }
.LBB0_327:
	v_lshl_add_u32 v174, s2, 8, v196
	s_cmp_eq_u32 s2, s43
	v_ashrrev_i32_e32 v175, 31, v174
	s_cbranch_scc1 .LBB0_345
	v_and_b32_e32 v135, 64, v210
	v_xor_b32_e32 v134, 16, v210
	v_add_u32_e32 v135, 64, v135
	v_cmp_lt_i32_e32 vcc, v134, v135
	v_cndmask_b32_e32 v134, v210, v134, vcc
	v_lshlrev_b32_e32 v161, 2, v134
	v_xor_b32_e32 v134, 32, v210
	v_cmp_lt_i32_e32 vcc, v134, v135
	v_cndmask_b32_e32 v134, v210, v134, vcc
	v_lshlrev_b32_e32 v162, 2, v134
	v_lshlrev_b64 v[132:133], 7, v[174:175]
	v_lshl_add_u64 v[132:133], v[168:169], 0, v[132:133]
	global_load_dwordx4 v[144:147], v[132:133], off
	global_load_dwordx4 v[148:151], v[132:133], off offset:16
	v_add_u32_e32 v132, 0x10, v174
	v_ashrrev_i32_e32 v133, 31, v132
	v_lshlrev_b64 v[132:133], 7, v[132:133]
	v_lshl_add_u64 v[132:133], v[168:169], 0, v[132:133]
	global_load_dwordx4 v[152:155], v[132:133], off
	global_load_dwordx4 v[156:159], v[132:133], off offset:16
	v_add_u32_e32 v132, 0x20, v174
	v_ashrrev_i32_e32 v133, 31, v132
	v_lshlrev_b64 v[132:133], 7, v[132:133]
	v_lshl_add_u64 v[132:133], v[168:169], 0, v[132:133]
	global_load_dwordx4 v[178:181], v[132:133], off
	global_load_dwordx4 v[182:185], v[132:133], off offset:16
	v_add_u32_e32 v132, 0x30, v174
	v_ashrrev_i32_e32 v133, 31, v132
	v_lshlrev_b64 v[132:133], 7, v[132:133]
	v_lshl_add_u64 v[132:133], v[168:169], 0, v[132:133]
	global_load_dwordx4 v[186:189], v[132:133], off
	global_load_dwordx4 v[190:193], v[132:133], off offset:16
	v_add_u32_e32 v132, 0x80, v174
	v_ashrrev_i32_e32 v133, 31, v132
	v_lshlrev_b64 v[132:133], 7, v[132:133]
	v_lshl_add_u64 v[132:133], v[168:169], 0, v[132:133]
	global_load_dwordx4 v[202:205], v[132:133], off
	global_load_dwordx4 v[206:209], v[132:133], off offset:16
	v_add_u32_e32 v132, 0x90, v174
	v_ashrrev_i32_e32 v133, 31, v132
	v_lshlrev_b64 v[132:133], 7, v[132:133]
	v_lshl_add_u64 v[132:133], v[168:169], 0, v[132:133]
	global_load_dwordx4 v[216:219], v[132:133], off
	global_load_dwordx4 v[220:223], v[132:133], off offset:16
	v_add_u32_e32 v132, 0xa0, v174
	v_ashrrev_i32_e32 v133, 31, v132
	v_lshlrev_b64 v[132:133], 7, v[132:133]
	v_lshl_add_u64 v[132:133], v[168:169], 0, v[132:133]
	global_load_dwordx4 v[224:227], v[132:133], off
	global_load_dwordx4 v[228:231], v[132:133], off offset:16
	v_add_u32_e32 v132, 0xb0, v174
	v_ashrrev_i32_e32 v133, 31, v132
	v_lshlrev_b64 v[132:133], 7, v[132:133]
	v_lshl_add_u64 v[132:133], v[168:169], 0, v[132:133]
	global_load_dwordx4 v[232:235], v[132:133], off
	global_load_dwordx4 v[236:239], v[132:133], off offset:16
	s_waitcnt vmcnt(14)
	v_add_f32_e32 v136, v144, v145
	v_add_f32_e32 v134, v146, v147
	v_add_f32_e32 v135, v148, v149
	v_add_f32_e32 v160, v150, v151
	v_add_f32_e32 v136, v136, v134
	v_add_f32_e32 v134, v135, v160
	v_add_f32_e32 v136, v136, v134
	ds_bpermute_b32 v240, v161, v136
	s_waitcnt vmcnt(12)
	v_add_f32_e32 v137, v152, v153
	v_add_f32_e32 v134, v154, v155
	v_add_f32_e32 v135, v156, v157
	v_add_f32_e32 v160, v158, v159
	v_add_f32_e32 v137, v137, v134
	v_add_f32_e32 v134, v135, v160
	v_add_f32_e32 v137, v137, v134
	ds_bpermute_b32 v241, v161, v137
	s_waitcnt vmcnt(10)
	v_add_f32_e32 v138, v178, v179
	v_add_f32_e32 v134, v180, v181
	v_add_f32_e32 v135, v182, v183
	v_add_f32_e32 v160, v184, v185
	v_add_f32_e32 v138, v138, v134
	v_add_f32_e32 v134, v135, v160
	v_add_f32_e32 v138, v138, v134
	ds_bpermute_b32 v242, v161, v138
	s_waitcnt vmcnt(8)
	v_add_f32_e32 v139, v186, v187
	v_add_f32_e32 v134, v188, v189
	v_add_f32_e32 v135, v190, v191
	v_add_f32_e32 v160, v192, v193
	v_add_f32_e32 v139, v139, v134
	v_add_f32_e32 v134, v135, v160
	v_add_f32_e32 v139, v139, v134
	ds_bpermute_b32 v243, v161, v139
	s_waitcnt vmcnt(6)
	v_add_f32_e32 v140, v202, v203
	v_add_f32_e32 v134, v204, v205
	v_add_f32_e32 v135, v206, v207
	v_add_f32_e32 v160, v208, v209
	v_add_f32_e32 v140, v140, v134
	v_add_f32_e32 v134, v135, v160
	v_add_f32_e32 v140, v140, v134
	ds_bpermute_b32 v244, v161, v140
	s_waitcnt vmcnt(4)
	v_add_f32_e32 v141, v216, v217
	v_add_f32_e32 v134, v218, v219
	v_add_f32_e32 v135, v220, v221
	v_add_f32_e32 v160, v222, v223
	v_add_f32_e32 v141, v141, v134
	v_add_f32_e32 v134, v135, v160
	v_add_f32_e32 v141, v141, v134
	ds_bpermute_b32 v245, v161, v141
	s_waitcnt vmcnt(2)
	v_add_f32_e32 v142, v224, v225
	v_add_f32_e32 v134, v226, v227
	v_add_f32_e32 v135, v228, v229
	v_add_f32_e32 v160, v230, v231
	v_add_f32_e32 v142, v142, v134
	v_add_f32_e32 v134, v135, v160
	v_add_f32_e32 v142, v142, v134
	ds_bpermute_b32 v246, v161, v142
	s_waitcnt vmcnt(0)
	v_add_f32_e32 v143, v232, v233
	v_add_f32_e32 v134, v234, v235
	v_add_f32_e32 v135, v236, v237
	v_add_f32_e32 v160, v238, v239
	v_add_f32_e32 v143, v143, v134
	v_add_f32_e32 v134, v135, v160
	v_add_f32_e32 v143, v143, v134
	ds_bpermute_b32 v247, v161, v143
	s_waitcnt lgkmcnt(0)
	v_add_f32_e32 v136, v136, v240
	ds_bpermute_b32 v240, v162, v136
	v_add_f32_e32 v137, v137, v241
	ds_bpermute_b32 v241, v162, v137
	v_add_f32_e32 v138, v138, v242
	ds_bpermute_b32 v242, v162, v138
	v_add_f32_e32 v139, v139, v243
	ds_bpermute_b32 v243, v162, v139
	v_add_f32_e32 v140, v140, v244
	ds_bpermute_b32 v244, v162, v140
	v_add_f32_e32 v141, v141, v245
	ds_bpermute_b32 v245, v162, v141
	v_add_f32_e32 v142, v142, v246
	ds_bpermute_b32 v246, v162, v142
	v_add_f32_e32 v143, v143, v247
	ds_bpermute_b32 v247, v162, v143
	s_and_saveexec_b64 s[4:5], s[6:7]
	s_cbranch_execz .Lrsfill_in_skip
	s_waitcnt lgkmcnt(0)
	v_add_f32_e32 v136, v136, v240
	v_fmamk_f32 v136, v136, 0x3a000000, v213
	v_rsq_f32_e32 v136, v136
	ds_write_b32 v199, v136
	v_add_f32_e32 v137, v137, v241
	v_fmamk_f32 v137, v137, 0x3a000000, v213
	v_rsq_f32_e32 v137, v137
	ds_write_b32 v199, v137 offset:64
	v_add_f32_e32 v138, v138, v242
	v_fmamk_f32 v138, v138, 0x3a000000, v213
	v_rsq_f32_e32 v138, v138
	ds_write_b32 v199, v138 offset:128
	v_add_f32_e32 v139, v139, v243
	v_fmamk_f32 v139, v139, 0x3a000000, v213
	v_rsq_f32_e32 v139, v139
	ds_write_b32 v199, v139 offset:192
	v_add_f32_e32 v140, v140, v244
	v_fmamk_f32 v140, v140, 0x3a000000, v213
	v_rsq_f32_e32 v140, v140
	ds_write_b32 v199, v140 offset:256
	v_add_f32_e32 v141, v141, v245
	v_fmamk_f32 v141, v141, 0x3a000000, v213
	v_rsq_f32_e32 v141, v141
	ds_write_b32 v199, v141 offset:320
	v_add_f32_e32 v142, v142, v246
	v_fmamk_f32 v142, v142, 0x3a000000, v213
	v_rsq_f32_e32 v142, v142
	ds_write_b32 v199, v142 offset:384
	v_add_f32_e32 v143, v143, v247
	v_fmamk_f32 v143, v143, 0x3a000000, v213
	v_rsq_f32_e32 v143, v143
	ds_write_b32 v199, v143 offset:448
.Lrsfill_in_skip:
	s_or_b64 exec, exec, s[4:5]
	s_waitcnt lgkmcnt(0)
	s_mov_b32 s43, s2
